# grid barrier second step: every workgroup polls the global arrival counter (target nx*(generation+1)); the XCD's last arriver flushes, adds 1 without a return value and waits like the others (no retur
# baseline (speedup 1.0000x reference)
.LBB0_296:
	s_or_b64 exec, exec, s[6:7]
	v_cvt_f32_u32_e32 v6, v4
	s_waitcnt vmcnt(0)
	v_readfirstlane_b32 s4, v5
	v_sub_u32_e32 v5, 0, v4
	v_rcp_iflag_f32_e32 v6, v6
	v_add_u32_e32 v7, s4, v3
	v_mul_f32_e32 v6, 0x4f7ffffe, v6
	v_cvt_u32_f32_e32 v6, v6
	v_mul_lo_u32 v3, v5, v6
	v_mul_hi_u32 v3, v6, v3
	v_add_u32_e32 v3, v6, v3
	v_mul_hi_u32 v3, v7, v3
	v_mul_lo_u32 v5, v3, v4
	v_sub_u32_e32 v5, v7, v5
	v_add_u32_e32 v6, 1, v3
	v_cmp_ge_u32_e32 vcc, v5, v4
	s_nop 1
	v_cndmask_b32_e32 v3, v3, v6, vcc
	v_sub_u32_e32 v6, v5, v4
	v_cndmask_b32_e32 v5, v5, v6, vcc
	v_add_u32_e32 v6, 1, v3
	v_cmp_ge_u32_e32 vcc, v5, v4
	v_add_u32_e32 v5, 1, v7
	s_nop 0
	v_cndmask_b32_e32 v3, v3, v6, vcc
	v_mul_lo_u32 v6, v4, v3
	v_add_u32_e32 v4, v6, v4
	v_cmp_ne_u32_e32 vcc, v5, v4
	s_waitcnt lgkmcnt(0)
	v_add_u32_e32 v249, 1, v3
	v_mul_lo_u32 v249, v249, v2
	s_cbranch_vccnz .Lbarw_1
	buffer_wbl2 sc1
	s_waitcnt vmcnt(0)
	v_mov_b32_e32 v247, 0x7000
	v_mov_b32_e32 v248, 1
	global_atomic_add v247, v248, s[56:57] offset:1024
	s_mov_b64 vcc, exec
.Lbarw_1:
	s_and_saveexec_b64 s[4:5], vcc
	s_xor_b64 s[4:5], exec, s[4:5]
	s_cbranch_execz .LBB0_310
	s_waitcnt lgkmcnt(0)
	v_mov_b32_e32 v2, 0x7000
	global_load_dword v2, v2, s[56:57] offset:1024 sc1
	s_add_u32 s14, s56, 0x7400
	s_addc_u32 s15, s57, 0
	s_waitcnt vmcnt(0)
	v_cmp_lt_u32_e32 vcc, v2, v249
	s_and_saveexec_b64 s[6:7], vcc
	s_cbranch_execz .LBB0_309
	s_add_u32 s8, s56, 0x4200
	s_addc_u32 s9, s57, 0
	s_mov_b32 s10, 1
	s_mov_b64 s[24:25], 0
	v_mov_b32_e32 v2, 0
	s_branch .LBB0_300

.LBB0_304:
	global_load_dword v4, v2, s[14:15] sc1
	s_add_i32 s10, s10, 1
	s_mov_b64 s[40:41], -1
	s_waitcnt vmcnt(0)
	v_cmp_ge_u32_e32 vcc, v4, v249
	s_orn2_b64 s[38:39], vcc, exec
	s_branch .LBB0_299

.Lbarw_2:
	s_and_saveexec_b64 s[4:5], vcc
	s_xor_b64 s[4:5], exec, s[4:5]
	s_cbranch_execz .LBB0_498
	s_waitcnt lgkmcnt(0)
	v_mov_b32_e32 v2, 0x7000
	global_load_dword v2, v2, s[56:57] offset:1024 sc1
	s_add_u32 s14, s56, 0x7400
	s_addc_u32 s15, s57, 0
	s_waitcnt vmcnt(0)
	v_cmp_lt_u32_e32 vcc, v2, v249
	s_and_saveexec_b64 s[6:7], vcc
	s_cbranch_execz .LBB0_497
	s_add_u32 s8, s56, 0x4200
	s_addc_u32 s9, s57, 0
	s_mov_b32 s10, 1
	s_mov_b64 s[36:37], 0
	v_mov_b32_e32 v2, 0
	s_branch .LBB0_488

.LBB0_492:
	global_load_dword v4, v2, s[14:15] sc1
	s_add_i32 s10, s10, 1
	s_mov_b64 s[44:45], -1
	s_waitcnt vmcnt(0)
	v_cmp_ge_u32_e32 vcc, v4, v249
	s_orn2_b64 s[42:43], vcc, exec
	s_branch .LBB0_487

.Lbarw_3:
	s_and_saveexec_b64 s[4:5], vcc
	s_xor_b64 s[4:5], exec, s[4:5]
	s_cbranch_execz .LBB0_580
	s_waitcnt lgkmcnt(0)
	v_mov_b32_e32 v2, 0x7000
	global_load_dword v2, v2, s[56:57] offset:1024 sc1
	s_add_u32 s14, s56, 0x7400
	s_addc_u32 s15, s57, 0
	s_waitcnt vmcnt(0)
	v_cmp_lt_u32_e32 vcc, v2, v249
	s_and_saveexec_b64 s[6:7], vcc
	s_cbranch_execz .LBB0_579
	s_add_u32 s8, s56, 0x4200
	s_addc_u32 s9, s57, 0
	s_mov_b32 s10, 1
	s_mov_b64 s[40:41], 0
	v_mov_b32_e32 v2, 0
	s_branch .LBB0_570

.LBB0_574:
	global_load_dword v4, v2, s[14:15] sc1
	s_add_i32 s10, s10, 1
	s_mov_b64 s[46:47], -1
	s_waitcnt vmcnt(0)
	v_cmp_ge_u32_e32 vcc, v4, v249
	s_orn2_b64 s[44:45], vcc, exec
	s_branch .LBB0_569

.Lbarw_4:
	s_and_saveexec_b64 s[4:5], vcc
	s_xor_b64 s[4:5], exec, s[4:5]
	s_cbranch_execz .LBB0_663
	s_waitcnt lgkmcnt(0)
	v_mov_b32_e32 v2, 0x7000
	global_load_dword v2, v2, s[56:57] offset:1024 sc1
	s_add_u32 s14, s56, 0x7400
	s_addc_u32 s15, s57, 0
	s_waitcnt vmcnt(0)
	v_cmp_lt_u32_e32 vcc, v2, v249
	s_and_saveexec_b64 s[6:7], vcc
	s_cbranch_execz .LBB0_662
	s_add_u32 s8, s56, 0x4200
	s_addc_u32 s9, s57, 0
	s_mov_b32 s10, 1
	s_mov_b64 s[22:23], 0
	v_mov_b32_e32 v2, 0
	s_branch .LBB0_653

.LBB0_657:
	global_load_dword v4, v2, s[14:15] sc1
	s_add_i32 s10, s10, 1
	s_mov_b64 s[30:31], -1
	s_waitcnt vmcnt(0)
	v_cmp_ge_u32_e32 vcc, v4, v249
	s_orn2_b64 s[28:29], vcc, exec
	s_branch .LBB0_652

.Lbarw_5:
	s_and_saveexec_b64 s[4:5], vcc
	s_xor_b64 s[4:5], exec, s[4:5]
	s_cbranch_execz .LBB0_818
	s_waitcnt lgkmcnt(0)
	v_mov_b32_e32 v2, 0x7000
	global_load_dword v2, v2, s[56:57] offset:1024 sc1
	s_add_u32 s14, s56, 0x7400
	s_addc_u32 s15, s57, 0
	s_waitcnt vmcnt(0)
	v_cmp_lt_u32_e32 vcc, v2, v249
	s_and_saveexec_b64 s[6:7], vcc
	s_cbranch_execz .LBB0_817
	s_add_u32 s8, s56, 0x4200
	s_addc_u32 s9, s57, 0
	s_mov_b32 s10, 1
	s_mov_b64 s[16:17], 0
	v_mov_b32_e32 v2, 0
	s_branch .LBB0_808

.Lbarw_6:
	s_and_saveexec_b64 s[4:5], vcc
	s_xor_b64 s[4:5], exec, s[4:5]
	s_cbranch_execz .LBB0_900
	s_waitcnt lgkmcnt(0)
	v_mov_b32_e32 v2, 0x7000
	global_load_dword v2, v2, s[56:57] offset:1024 sc1
	s_add_u32 s14, s56, 0x7400
	s_addc_u32 s15, s57, 0
	s_waitcnt vmcnt(0)
	v_cmp_lt_u32_e32 vcc, v2, v249
	s_and_saveexec_b64 s[6:7], vcc
	s_cbranch_execz .LBB0_899
	s_add_u32 s8, s56, 0x4200
	s_addc_u32 s9, s57, 0
	s_mov_b32 s10, 1
	s_mov_b64 s[26:27], 0
	v_mov_b32_e32 v2, 0
	s_branch .LBB0_890

.LBB0_894:
	global_load_dword v4, v2, s[14:15] sc1
	s_add_i32 s10, s10, 1
	s_mov_b64 s[40:41], -1
	s_waitcnt vmcnt(0)
	v_cmp_ge_u32_e32 vcc, v4, v249
	s_orn2_b64 s[30:31], vcc, exec
	s_branch .LBB0_889

.LBB0_1049:
	global_load_dword v4, v2, s[14:15] sc1
	s_add_i32 s10, s10, 1
	s_mov_b64 s[28:29], -1
	s_waitcnt vmcnt(0)
	v_cmp_ge_u32_e32 vcc, v4, v249
	s_orn2_b64 s[26:27], vcc, exec
	s_branch .LBB0_1044

.LBB0_1251:
	s_or_b64 exec, exec, s[8:9]
	v_cvt_f32_u32_e32 v6, v4
	s_waitcnt vmcnt(0)
	v_readfirstlane_b32 s6, v5
	v_sub_u32_e32 v5, 0, v4
	v_rcp_iflag_f32_e32 v6, v6
	v_add_u32_e32 v7, s6, v3
	v_mul_f32_e32 v6, 0x4f7ffffe, v6
	v_cvt_u32_f32_e32 v6, v6
	v_mul_lo_u32 v3, v5, v6
	v_mul_hi_u32 v3, v6, v3
	v_add_u32_e32 v3, v6, v3
	v_mul_hi_u32 v3, v7, v3
	v_mul_lo_u32 v5, v3, v4
	v_sub_u32_e32 v5, v7, v5
	v_add_u32_e32 v6, 1, v3
	v_cmp_ge_u32_e32 vcc, v5, v4
	s_nop 1
	v_cndmask_b32_e32 v3, v3, v6, vcc
	v_sub_u32_e32 v6, v5, v4
	v_cndmask_b32_e32 v5, v5, v6, vcc
	v_add_u32_e32 v6, 1, v3
	v_cmp_ge_u32_e32 vcc, v5, v4
	v_add_u32_e32 v5, 1, v7
	s_nop 0
	v_cndmask_b32_e32 v3, v3, v6, vcc
	v_mul_lo_u32 v6, v4, v3
	v_add_u32_e32 v4, v6, v4
	v_cmp_ne_u32_e32 vcc, v5, v4
	s_waitcnt lgkmcnt(0)
	v_add_u32_e32 v249, 1, v3
	v_mul_lo_u32 v249, v249, v2
	s_cbranch_vccnz .Lbarw_9
	buffer_wbl2 sc1
	s_waitcnt vmcnt(0)
	v_mov_b32_e32 v247, 0x7000
	v_mov_b32_e32 v248, 1
	global_atomic_add v247, v248, s[56:57] offset:1024
	s_mov_b64 vcc, exec
.Lbarw_9:
	s_and_saveexec_b64 s[6:7], vcc
	s_xor_b64 s[6:7], exec, s[6:7]
	s_cbranch_execz .LBB0_1265
	s_waitcnt lgkmcnt(0)
	v_mov_b32_e32 v2, 0x7000
	global_load_dword v2, v2, s[56:57] offset:1024 sc1
	s_add_u32 s16, s56, 0x7400
	s_addc_u32 s17, s57, 0
	s_waitcnt vmcnt(0)
	v_cmp_lt_u32_e32 vcc, v2, v249
	s_and_saveexec_b64 s[8:9], vcc
	s_cbranch_execz .LBB0_1264
	s_add_u32 s14, s56, 0x4200
	s_addc_u32 s15, s57, 0
	s_mov_b32 s10, 1
	s_mov_b64 s[18:19], 0
	v_mov_b32_e32 v2, 0
	s_branch .LBB0_1255

.LBB0_1259:
	global_load_dword v4, v2, s[16:17] sc1
	s_add_i32 s10, s10, 1
	s_mov_b64 s[30:31], -1
	s_waitcnt vmcnt(0)
	v_cmp_ge_u32_e32 vcc, v4, v249
	s_orn2_b64 s[28:29], vcc, exec
	s_branch .LBB0_1254

.LBB0_1417:
	global_load_dword v4, v2, s[14:15] sc1
	s_add_i32 s10, s10, 1
	s_mov_b64 s[26:27], -1
	s_waitcnt vmcnt(0)
	v_cmp_ge_u32_e32 vcc, v4, v249
	s_orn2_b64 s[20:21], vcc, exec
	s_branch .LBB0_1412

.LBB0_1487:
	global_load_dword v4, v2, s[14:15] sc1
	s_add_i32 s10, s10, 1
	s_mov_b64 s[30:31], -1
	s_waitcnt vmcnt(0)
	v_cmp_ge_u32_e32 vcc, v4, v249
	s_orn2_b64 s[24:25], vcc, exec
	s_branch .LBB0_1482

.Lbarw_14:
	s_and_saveexec_b64 s[4:5], vcc
	s_xor_b64 s[4:5], exec, s[4:5]
	s_cbranch_execz .LBB0_1656
	s_waitcnt lgkmcnt(0)
	v_mov_b32_e32 v2, 0x7000
	global_load_dword v2, v2, s[56:57] offset:1024 sc1
	s_add_u32 s10, s56, 0x7400
	s_addc_u32 s11, s57, 0
	s_waitcnt vmcnt(0)
	v_cmp_lt_u32_e32 vcc, v2, v249
	s_and_saveexec_b64 s[6:7], vcc
	s_cbranch_execz .LBB0_1655
	s_add_u32 s8, s56, 0x4200
	s_addc_u32 s9, s57, 0
	s_mov_b32 s28, 1
	s_mov_b64 s[12:13], 0
	v_mov_b32_e32 v2, 0
	s_branch .LBB0_1646

.LBB0_1650:
	global_load_dword v4, v2, s[10:11] sc1
	s_add_i32 s28, s28, 1
	s_mov_b64 s[18:19], -1
	s_waitcnt vmcnt(0)
	v_cmp_ge_u32_e32 vcc, v4, v249
	s_orn2_b64 s[16:17], vcc, exec
	s_branch .LBB0_1645
